# grid barrier release poll: s_sleep between polls removed (shorter serial chain at the release edge)
# baseline (speedup 1.0000x reference)
.Lxbn_0:
	global_load_dword v5, v4, s[2:3] offset:1024 sc1
	s_waitcnt vmcnt(0)
	v_sub_u32_e32 v5, v5, v3
	v_cmp_gt_i32_e32 vcc, 0, v5
	s_cbranch_vccz .Lxbnd_0
	s_add_u32 s26, s26, 1
	s_cmp_lt_u32 s26, 0x100000
	s_cbranch_scc1 .Lxbn_0

.Lxbn_1:
	global_load_dword v5, v4, s[2:3] offset:1024 sc1
	s_waitcnt vmcnt(0)
	v_sub_u32_e32 v5, v5, v3
	v_cmp_gt_i32_e32 vcc, 0, v5
	s_cbranch_vccz .Lxbnd_1
	s_add_u32 s22, s22, 1
	s_cmp_lt_u32 s22, 0x100000
	s_cbranch_scc1 .Lxbn_1

.Lxbn_6:
	global_load_dword v5, v4, s[4:5] offset:1024 sc1
	s_waitcnt vmcnt(0)
	v_sub_u32_e32 v5, v5, v3
	v_cmp_gt_i32_e32 vcc, 0, v5
	s_cbranch_vccz .Lxbnd_6
	s_add_u32 s24, s24, 1
	s_cmp_lt_u32 s24, 0x100000
	s_cbranch_scc1 .Lxbn_6

.Lxbn_11:
	global_load_dword v6, v5, s[2:3] offset:1024 sc1
	s_waitcnt vmcnt(0)
	v_sub_u32_e32 v6, v6, v4
	v_cmp_gt_i32_e32 vcc, 0, v6
	s_cbranch_vccz .Lxbnd_11
	s_add_u32 s22, s22, 1
	s_cmp_lt_u32 s22, 0x100000
	s_cbranch_scc1 .Lxbn_11

.Lxbn_13:
	global_load_dword v6, v5, s[4:5] offset:1024 sc1
	s_waitcnt vmcnt(0)
	v_sub_u32_e32 v6, v6, v4
	v_cmp_gt_i32_e32 vcc, 0, v6
	s_cbranch_vccz .Lxbnd_13
	s_add_u32 s26, s26, 1
	s_cmp_lt_u32 s26, 0x100000
	s_cbranch_scc1 .Lxbn_13

.Lxbn_14:
	global_load_dword v6, v5, s[4:5] offset:1024 sc1
	s_waitcnt vmcnt(0)
	v_sub_u32_e32 v6, v6, v4
	v_cmp_gt_i32_e32 vcc, 0, v6
	s_cbranch_vccz .Lxbnd_14
	s_add_u32 s24, s24, 1
	s_cmp_lt_u32 s24, 0x100000
	s_cbranch_scc1 .Lxbn_14
